# v41 stack + layer-0 gate/up GEMM unit-boundary hosting of list conversion items (1/4 of workgroups per boundary)
# speedup vs baseline: 1.0030x; 1.0030x over previous
; #define PG8_BAR __builtin_amdgcn_s_barrier()
; template <class Epi, class Sched, bool ALIGN_EPI = false, bool SP2 = false, bool F8 = false, bool BTILED = false, bool ATILED = false>
; __device__ __forceinline__ void gemm_phase(PG8_LAS unsigned char* lds, const Gemm g, const Sched& S, const Epi& E) {
;     ...
;         if constexpr (!Epi::AFTER_DRAIN) { E(acc, cur, wr, wc, fr, fq); S.done(cur); }
;         if (!has_next) break;
; #pragma unroll
;         for (int a = 0; a < 2; ++a)
; #pragma unroll
;             for (int b = 0; b < 2; ++b)
; #pragma unroll
;                 for (int m = 0; m < 4; ++m)
; #pragma unroll
;                     for (int n = 0; n < 2; ++n) acc[a][b][m][n] = (f32x4){0.f, 0.f, 0.f, 0.f};
;         cur = nxt; cA = nA; cB = nB; ++ui;
;         if constexpr (ALIGN_EPI) { if (wr == 1) PG8_BAR; }
;     }
.LBB0_1653:
	s_andn2_b64 vcc, exec, s[2:3]
	s_mov_b32 s43, s42
	s_mov_b32 s18, s10
	s_mov_b64 s[2:3], s[16:17]
	s_mov_b64 s[20:21], s[14:15]
	s_cbranch_vccz .LBB0_1663
	s_cmp_lg_u32 s54, 0
	s_cbranch_scc1 .Lh_skip
	s_add_u32 s100, s41, s88
	s_and_b32 s100, s100, 3
	s_cmp_lg_u32 s100, 0
	s_cbranch_scc1 .Lh_skip0
	v_writelane_b32 v222, s0, 0
	v_writelane_b32 v222, s1, 1
	v_writelane_b32 v222, s2, 2
	v_writelane_b32 v222, s3, 3
	v_writelane_b32 v222, s4, 4
	v_writelane_b32 v222, s5, 5
	v_writelane_b32 v222, s6, 6
	v_writelane_b32 v222, s7, 7
	v_writelane_b32 v222, s8, 8
	v_writelane_b32 v222, s9, 9
	v_writelane_b32 v222, s10, 10
	v_writelane_b32 v222, s11, 11
	v_writelane_b32 v222, s12, 12
	v_writelane_b32 v222, s13, 13
	v_writelane_b32 v222, s14, 14
	v_writelane_b32 v222, s15, 15
	v_writelane_b32 v222, s16, 16
	v_writelane_b32 v222, s17, 17
	v_writelane_b32 v222, s18, 18
	v_writelane_b32 v222, s19, 19
	v_writelane_b32 v222, s20, 20
	v_writelane_b32 v222, s21, 21
	v_writelane_b32 v222, s22, 22
	v_writelane_b32 v222, s23, 23
	v_writelane_b32 v222, s89, 24
	v_writelane_b32 v222, s94, 25
	v_mov_b32_e32 v223, v1
	v_mov_b32_e32 v221, v182
	s_mov_b32 s100, 0x1234
	s_branch .Lfl_entry
